# nt cache hint on LN0 input loads, LN2 loads and LN2 f32 output stores
# speedup vs baseline: 1.0030x; 1.0030x over previous
; __device__ __forceinline__ void ph_prologue(const Params& p, LAS unsigned char* lds, const int wvid) {
;     ...
;     const LnPar ln0 = ln_par(p.in[I_LN0G], p.in[I_LN0B], lane);
;     auto row_src = [&](int r) -> const float* { const int rc = r < T ? r : 0; const int b = rc / LT, t = rc % LT; return t < NMETA ? p.in[I_META] + (size_t)t * D : p.in[I_X] + ((size_t)b * SEQ + (t - NMETA)) * D; };
;     f32x4 vn[4];
;     { const float* src = row_src(gw);
; #pragma unroll
;       for (int j = 0; j < 4; ++j) vn[j] = *(const f32x4*)(src + 4 * lane + 256 * j); }
;     for (int r = gw; r < MP; r += NGW) {
;         f32x4 v[4];
;         { const float* src = row_src(r + NGW < MP ? r + NGW : r);
; #pragma unroll
;           for (int j = 0; j < 4; ++j) { v[j] = vn[j]; vn[j] = *(const f32x4*)(src + 4 * lane + 256 * j); } }
.LBB0_38:
	s_andn2_saveexec_b64 s[0:1], s[0:1]
	v_ashrrev_i32_e32 v33, 31, v32
	s_or_b64 exec, exec, s[0:1]
	s_mov_b32 s10, 0x8100
	v_cmp_gt_i32_e32 vcc, s10, v64
	s_and_saveexec_b64 s[2:3], vcc
	s_cbranch_execz .LBB0_51
	v_lshlrev_b32_e32 v37, 2, v40
	s_waitcnt vmcnt(9)
	v_lshlrev_b32_e32 v66, 1, v37
	v_mov_b32_e32 v67, 0
	v_lshlrev_b64 v[32:33], 12, v[32:33]
	v_lshl_add_u64 v[38:39], s[4:5], 0, v[66:67]
	v_lshl_add_u64 v[32:33], v[34:35], 0, v[32:33]
	v_lshlrev_b32_e32 v66, 2, v37
	v_lshl_add_u64 v[42:43], v[32:33], 0, v[66:67]
	global_load_dwordx4 v[32:35], v[42:43], off offset:3072 nt
	global_load_dwordx4 v[44:47], v[42:43], off offset:2048 nt
	global_load_dwordx4 v[56:59], v[42:43], off offset:1024 nt
	global_load_dwordx4 v[60:63], v[42:43], off nt
	v_ashrrev_i32_e32 v37, 31, v36
	s_ashr_i32 s7, s6, 31
	v_lshl_add_u64 v[36:37], v[36:37], 0, s[6:7]
	v_lshlrev_b64 v[36:37], 11, v[36:37]
	s_mov_b64 s[0:1], 0xf1f0000
	v_lshl_or_b32 v36, v40, 3, v36
	v_lshl_add_u64 v[68:69], v[38:39], 0, s[0:1]
	v_lshl_add_u64 v[36:37], s[4:5], 0, v[36:37]
	s_mov_b64 s[0:1], 0x10400
	s_ashr_i32 s81, s80, 31
	v_lshl_add_u64 v[70:71], v[36:37], 0, s[0:1]
	s_lshl_b64 s[4:5], s[80:81], 11
	s_mov_b64 s[6:7], 0
	s_mov_b32 s11, 0x80ff
	s_mov_b32 s12, 0x8080
	s_mov_b32 s13, 0x7f807f81
	v_mov_b32_e32 v80, 0x3727c5ac
	s_movk_i32 s14, 0x7fff
	s_mov_b32 s15, 0xffff0000
	v_mov_b32_e32 v81, 0xba800000
	v_mov_b32_e32 v82, 0x3a800000
	s_mov_b32 s8, 0
	s_branch .LBB0_43

; __device__ __forceinline__ float frsq(float x) { return __builtin_amdgcn_rsqf(x); }
; __device__ __forceinline__ void ln_affine(f32x4 (&v)[4], const LnPar& q) {
;     float s = 0.f;
; #pragma unroll
;     for (int j = 0; j < 4; ++j) s += (v[j][0] + v[j][1]) + (v[j][2] + v[j][3]);
;     const float mean = wave_sum(s) * (1.f / D); float s2 = 0.f;
; #pragma unroll
;     for (int j = 0; j < 4; ++j) { v[j] = v[j] - mean; s2 += (v[j][0] * v[j][0] + v[j][1] * v[j][1]) + (v[j][2] * v[j][2] + v[j][3] * v[j][3]); }
;     const float rstd = frsq(wave_sum(s2) * (1.f / D) + 1e-5f);
; #pragma unroll
;     for (int j = 0; j < 4; ++j) v[j] = v[j] * rstd * q.g[j] + q.b[j];
; }
; __device__ __forceinline__ void ph_prologue(const Params& p, LAS unsigned char* lds, const int wvid) {
;     ...
;     for (int r = gw; r < MP; r += NGW) {
;         f32x4 v[4];
;         { const float* src = row_src(r + NGW < MP ? r + NGW : r);
; #pragma unroll
;           for (int j = 0; j < 4; ++j) { v[j] = vn[j]; vn[j] = *(const f32x4*)(src + 4 * lane + 256 * j); } }
;         if (r >= T) {
; #pragma unroll
;             for (int j = 0; j < 4; ++j) v[j] = (f32x4){0.f, 0.f, 0.f, 0.f};
;             store_row_bf16(MIX + (size_t)r * D, v, lane);
;         } else ln_affine(v, ln0);
;         store_row_bf16(HB + (size_t)r * D, v, lane);
.LBB0_45:
	s_andn2_saveexec_b64 s[0:1], s[0:1]
	v_ashrrev_i32_e32 v37, 31, v36
	s_or_b64 exec, exec, s[0:1]
	v_lshlrev_b64 v[36:37], 12, v[36:37]
	v_lshl_add_u64 v[36:37], v[40:41], 0, v[36:37]
	v_lshl_add_u64 v[52:53], v[36:37], 0, v[66:67]
	global_load_dwordx4 v[36:39], v[52:53], off nt
	global_load_dwordx4 v[40:43], v[52:53], off offset:1024 nt
	global_load_dwordx4 v[48:51], v[52:53], off offset:2048 nt
	s_nop 0
	global_load_dwordx4 v[52:55], v[52:53], off offset:3072 nt
	v_cmp_gt_i32_e64 s[0:1], s12, v64
	s_and_saveexec_b64 s[16:17], s[0:1]
	s_xor_b64 s[0:1], exec, s[16:17]
	s_cbranch_execz .LBB0_49
	s_waitcnt vmcnt(4)
	v_mov_b32_e32 v64, v61
	v_mov_b32_e32 v65, v62
	v_mov_b32_e32 v72, v60
	v_mov_b32_e32 v73, v63
	v_pk_add_f32 v[64:65], v[64:65], v[72:73]
	v_mov_b32_e32 v72, v57
	v_mov_b32_e32 v73, v58
	v_mov_b32_e32 v74, v56
	v_mov_b32_e32 v75, v59
	v_pk_add_f32 v[72:73], v[72:73], v[74:75]
	v_add_f32_e32 v64, v64, v65
	v_pk_add_f32 v[72:73], v[72:73], v[72:73] op_sel_hi:[0,1]
	v_add_f32_e32 v65, 0, v64
	v_add_f32_e32 v75, v44, v45
	v_add_f32_e32 v77, v46, v47
	v_mov_b32_e32 v74, v32
	v_mov_b32_e32 v76, v33
	v_mov_b32_e32 v72, v34
	v_mov_b32_e32 v64, v35
	v_pk_add_f32 v[74:75], v[74:75], v[76:77]
	v_pk_add_f32 v[64:65], v[72:73], v[64:65]
	s_nop 0
	v_pk_add_f32 v[64:65], v[74:75], v[64:65]
	s_nop 0
	v_add_f32_e32 v64, v64, v65
	v_mov_b32_e32 v65, v67
	s_nop 0
	v_add_f32_dpp v64, v64, v64 quad_perm:[1,0,3,2] row_mask:0xf bank_mask:0xf bound_ctrl:1
	s_nop 1
	v_add_f32_dpp v64, v64, v64 quad_perm:[2,3,0,1] row_mask:0xf bank_mask:0xf bound_ctrl:1
	s_nop 1
	v_add_f32_dpp v64, v64, v64 row_half_mirror row_mask:0xf bank_mask:0xf bound_ctrl:1
	s_nop 1
	v_add_f32_dpp v64, v64, v64 row_mirror row_mask:0xf bank_mask:0xf bound_ctrl:1
	s_nop 1
	v_mov_b32_dpp v65, v64 row_bcast:15 row_mask:0xa bank_mask:0xf
	v_add_f32_e32 v64, v64, v65
	v_mov_b32_e32 v65, v67
	s_nop 1
	v_mov_b32_dpp v65, v64 row_bcast:31 row_mask:0xc bank_mask:0xf
	v_add_f32_e32 v64, v64, v65
	s_nop 0
	v_readlane_b32 s9, v64, 63
	s_nop 1
	v_fma_f32 v61, s9, v81, v61
	v_fma_f32 v60, s9, v81, v60
	v_fma_f32 v63, s9, v81, v63
	v_fmac_f32_e32 v62, s9, v81
	v_pk_mul_f32 v[64:65], v[62:63], v[62:63]
	v_pk_mul_f32 v[72:73], v[60:61], v[60:61]
	v_fma_f32 v57, s9, v81, v57
	v_pk_mov_b32 v[74:75], v[72:73], v[64:65] op_sel:[1,0]
	v_mov_b32_e32 v73, v65
	v_pk_add_f32 v[64:65], v[74:75], v[72:73]
	v_fma_f32 v56, s9, v81, v56
	v_fma_f32 v59, s9, v81, v59
	v_fmac_f32_e32 v58, s9, v81
	v_pk_add_f32 v[64:65], v[64:65], v[64:65] op_sel_hi:[0,1]
	v_pk_mul_f32 v[72:73], v[58:59], v[58:59]
	v_pk_mul_f32 v[74:75], v[56:57], v[56:57]
	v_fma_f32 v44, s9, v81, v44
	v_pk_mov_b32 v[76:77], v[74:75], v[72:73] op_sel:[1,0]
	v_mov_b32_e32 v75, v73
	v_fma_f32 v45, s9, v81, v45
	v_fmac_f32_e32 v46, s9, v81
	v_mul_f32_e32 v64, v44, v44
	v_pk_add_f32 v[72:73], v[76:77], v[74:75]
	v_fma_f32 v47, s9, v81, v47
	v_pk_fma_f32 v[74:75], v[44:45], v[44:45], v[64:65] op_sel_hi:[1,1,0]
	v_mul_f32_e32 v64, v46, v46
	v_pk_add_f32 v[72:73], v[72:73], v[72:73] op_sel_hi:[0,1]
	v_pk_fma_f32 v[76:77], v[46:47], v[46:47], v[64:65] op_sel_hi:[1,1,0]
	v_fma_f32 v35, s9, v81, v35
	v_fma_f32 v34, s9, v81, v34
	v_fma_f32 v33, s9, v81, v33
	v_fmac_f32_e32 v32, s9, v81
	v_mul_f32_e32 v74, v32, v32
	v_mul_f32_e32 v76, v33, v33
	v_mul_f32_e32 v64, v34, v34
	v_mul_f32_e32 v72, v35, v35
	v_pk_add_f32 v[74:75], v[74:75], v[76:77]
	v_pk_add_f32 v[64:65], v[64:65], v[72:73]
	s_nop 0
	v_pk_add_f32 v[64:65], v[74:75], v[64:65]
	s_nop 0
	v_add_f32_e32 v64, v64, v65
	v_mov_b32_e32 v65, v67
	s_nop 0
	v_add_f32_dpp v64, v64, v64 quad_perm:[1,0,3,2] row_mask:0xf bank_mask:0xf bound_ctrl:1
	s_nop 1
	v_add_f32_dpp v64, v64, v64 quad_perm:[2,3,0,1] row_mask:0xf bank_mask:0xf bound_ctrl:1
	s_nop 1
	v_add_f32_dpp v64, v64, v64 row_half_mirror row_mask:0xf bank_mask:0xf bound_ctrl:1
	s_nop 1
	v_add_f32_dpp v64, v64, v64 row_mirror row_mask:0xf bank_mask:0xf bound_ctrl:1
	s_nop 1
	v_mov_b32_dpp v65, v64 row_bcast:15 row_mask:0xa bank_mask:0xf
	v_add_f32_e32 v64, v64, v65
	v_mov_b32_e32 v65, v67
	s_nop 1
	v_mov_b32_dpp v65, v64 row_bcast:31 row_mask:0xc bank_mask:0xf
	v_add_f32_e32 v64, v64, v65
	s_nop 0
	v_readlane_b32 s9, v64, 63
	s_nop 1
	v_fma_f32 v64, s9, v82, v80
	v_rsq_f32_e32 v64, v64
	s_nop 0
	v_pk_mul_f32 v[60:61], v[60:61], v[64:65] op_sel_hi:[1,0]
	s_nop 0
	v_pk_fma_f32 v[60:61], v[0:1], v[60:61], v[4:5]
	v_pk_mul_f32 v[62:63], v[62:63], v[64:65] op_sel_hi:[1,0]
	v_pk_mul_f32 v[56:57], v[56:57], v[64:65] op_sel_hi:[1,0]
	v_pk_mul_f32 v[58:59], v[58:59], v[64:65] op_sel_hi:[1,0]
	v_pk_mul_f32 v[44:45], v[44:45], v[64:65] op_sel_hi:[1,0]
	v_pk_mul_f32 v[46:47], v[46:47], v[64:65] op_sel_hi:[1,0]
	v_pk_mul_f32 v[32:33], v[32:33], v[64:65] op_sel_hi:[1,0]
	v_pk_mul_f32 v[34:35], v[34:35], v[64:65] op_sel_hi:[1,0]
	v_bfe_u32 v64, v60, 16, 1
	v_add3_u32 v60, v60, v64, s14
	v_bfe_u32 v64, v61, 16, 1
	v_pk_fma_f32 v[62:63], v[2:3], v[62:63], v[6:7]
	v_lshrrev_b32_e32 v60, 16, v60
	v_add3_u32 v61, v61, v64, s14
	v_and_or_b32 v72, v61, s15, v60
	v_bfe_u32 v60, v62, 16, 1
	v_add3_u32 v60, v62, v60, s14
	v_bfe_u32 v61, v63, 16, 1
	v_pk_fma_f32 v[56:57], v[8:9], v[56:57], v[12:13]
	v_lshrrev_b32_e32 v60, 16, v60
	v_add3_u32 v61, v63, v61, s14
	v_and_or_b32 v73, v61, s15, v60
	v_bfe_u32 v60, v56, 16, 1
	v_add3_u32 v56, v56, v60, s14
	v_bfe_u32 v60, v57, 16, 1
	v_pk_fma_f32 v[58:59], v[10:11], v[58:59], v[14:15]
	v_lshrrev_b32_e32 v56, 16, v56
	v_add3_u32 v57, v57, v60, s14
	v_and_or_b32 v74, v57, s15, v56
	v_bfe_u32 v56, v58, 16, 1
	v_add3_u32 v56, v58, v56, s14
	v_bfe_u32 v57, v59, 16, 1
	v_pk_fma_f32 v[44:45], v[16:17], v[44:45], v[20:21]
	v_lshrrev_b32_e32 v56, 16, v56
	v_add3_u32 v57, v59, v57, s14
	v_and_or_b32 v75, v57, s15, v56
	v_bfe_u32 v56, v44, 16, 1
	v_add3_u32 v44, v44, v56, s14
	v_bfe_u32 v56, v45, 16, 1
	v_pk_fma_f32 v[46:47], v[18:19], v[46:47], v[22:23]
	v_lshrrev_b32_e32 v44, 16, v44
	v_add3_u32 v45, v45, v56, s14
	v_and_or_b32 v76, v45, s15, v44
	v_bfe_u32 v44, v46, 16, 1
	v_add3_u32 v44, v46, v44, s14
	v_bfe_u32 v45, v47, 16, 1
	v_pk_fma_f32 v[32:33], v[24:25], v[32:33], v[28:29]
	v_lshrrev_b32_e32 v44, 16, v44
	v_add3_u32 v45, v47, v45, s14
	v_and_or_b32 v77, v45, s15, v44
	v_bfe_u32 v44, v32, 16, 1
	v_add3_u32 v32, v32, v44, s14
	v_bfe_u32 v44, v33, 16, 1
	v_pk_fma_f32 v[34:35], v[26:27], v[34:35], v[30:31]
	v_lshrrev_b32_e32 v32, 16, v32
	v_add3_u32 v33, v33, v44, s14
	v_and_or_b32 v78, v33, s15, v32
	v_bfe_u32 v32, v34, 16, 1
	v_add3_u32 v32, v34, v32, s14
	v_bfe_u32 v33, v35, 16, 1
	v_lshrrev_b32_e32 v32, 16, v32
	v_add3_u32 v33, v35, v33, s14
	v_and_or_b32 v79, v33, s15, v32

; __device__ __forceinline__ void ph_ln2(const Params& p, int l, LAS unsigned char* lds, const int wvid) {
;     ...
;     for (int r = gw; r < T; r += 4 * NGW, k += 4) {
;         u32x2 hv[4][4], av[4][4], cv[4][4]; bool on[4];
; #pragma unroll
;         for (int q = 0; q < 4; ++q) { const int rr = r + q * NGW; const int t = rr % LT; on[q] = rr < T && !(l == NLAYER - 1 && t < NMETA);
;             const int rc = rr < T ? rr : gw; const int s0 = __builtin_amdgcn_readlane(sl0, k + q), s1 = __builtin_amdgcn_readlane(sl1, k + q);
; #pragma unroll
;             for (int j = 0; j < 4; ++j) { hv[q][j] = *(const u32x2*)(HB + (size_t)rc * D + 4 * lane + 256 * j); av[q][j] = *(const u32x2*)(Y2 + (size_t)s0 * D + 4 * lane + 256 * j); cv[q][j] = *(const u32x2*)(Y2 + (size_t)s1 * D + 4 * lane + 256 * j); } }
.LBB0_1637:
	v_readlane_b32 s6, v51, s8
	v_readlane_b32 s10, v148, s8
	v_ashrrev_i32_e32 v57, 31, v56
	s_ashr_i32 s7, s6, 31
	s_waitcnt vmcnt(36)
	v_lshlrev_b64 v[34:35], 11, v[56:57]
	s_lshl_b64 s[6:7], s[6:7], 11
	s_ashr_i32 s11, s10, 31
	v_lshl_add_u64 v[118:119], v[52:53], 0, v[34:35]
	v_lshl_add_u64 v[34:35], v[54:55], 0, s[6:7]
	s_lshl_b64 s[6:7], s[10:11], 11
	v_lshl_add_u64 v[58:59], v[54:55], 0, s[6:7]
	global_load_dwordx2 v[142:143], v[118:119], off nt
	global_load_dwordx2 v[46:47], v[118:119], off offset:512 nt
	global_load_dwordx2 v[40:41], v[118:119], off offset:1024 nt
	global_load_dwordx2 v[36:37], v[118:119], off offset:1536 nt
	global_load_dwordx2 v[146:147], v[34:35], off nt
	global_load_dwordx2 v[140:141], v[34:35], off offset:512 nt
	global_load_dwordx2 v[44:45], v[34:35], off offset:1024 nt
	global_load_dwordx2 v[38:39], v[34:35], off offset:1536 nt
	global_load_dwordx2 v[144:145], v[58:59], off nt
	global_load_dwordx2 v[48:49], v[58:59], off offset:512 nt
	global_load_dwordx2 v[42:43], v[58:59], off offset:1024 nt
	s_nop 0
	global_load_dwordx2 v[34:35], v[58:59], off offset:1536 nt
	v_add_u32_e32 v98, s80, v56
	s_mov_b32 s6, 0x8080
	v_cmp_gt_i32_e32 vcc, s6, v98
	s_mov_b64 s[10:11], 0
	v_mov_b32_e32 v58, v50
	s_and_saveexec_b64 s[6:7], vcc
	s_cbranch_execz .LBB0_1639
	s_mov_b32 s9, 0x7f807f81
	v_mul_hi_i32 v0, v98, s9
	v_lshrrev_b32_e32 v57, 31, v0
	v_ashrrev_i32_e32 v0, 11, v0
	v_add_u32_e32 v0, v0, v57
	v_mul_i32_i24_e32 v0, 0x1010, v0
	v_sub_u32_e32 v0, v98, v0
	v_readlane_b32 s10, v254, 52
	v_cmp_lt_i32_e32 vcc, 15, v0
	v_readlane_b32 s11, v254, 53
	s_or_b64 s[10:11], s[10:11], vcc
	s_and_b64 s[10:11], s[10:11], exec
	v_mov_b32_e32 v58, v98
.LBB0_1639:
	s_or_b64 exec, exec, s[6:7]
	s_add_i32 s20, s8, 1
	v_readlane_b32 s6, v51, s20
	v_readlane_b32 s8, v148, s20
	v_ashrrev_i32_e32 v59, 31, v58
	s_ashr_i32 s7, s6, 31
	v_lshlrev_b64 v[58:59], 11, v[58:59]
	s_lshl_b64 s[6:7], s[6:7], 11
	s_ashr_i32 s9, s8, 31
	v_lshl_add_u64 v[58:59], v[52:53], 0, v[58:59]
	s_waitcnt vmcnt(12)
	v_lshl_add_u64 v[60:61], v[54:55], 0, s[6:7]
	s_lshl_b64 s[6:7], s[8:9], 11
	v_lshl_add_u64 v[62:63], v[54:55], 0, s[6:7]
	global_load_dwordx2 v[132:133], v[58:59], off nt
	global_load_dwordx2 v[126:127], v[58:59], off offset:512 nt
	global_load_dwordx2 v[120:121], v[58:59], off offset:1024 nt
	global_load_dwordx2 v[114:115], v[58:59], off offset:1536 nt
	global_load_dwordx2 v[136:137], v[60:61], off nt
	global_load_dwordx2 v[130:131], v[60:61], off offset:512 nt
	global_load_dwordx2 v[124:125], v[60:61], off offset:1024 nt
	global_load_dwordx2 v[116:117], v[60:61], off offset:1536 nt
	global_load_dwordx2 v[134:135], v[62:63], off nt
	global_load_dwordx2 v[128:129], v[62:63], off offset:512 nt
	global_load_dwordx2 v[122:123], v[62:63], off offset:1024 nt
	global_load_dwordx2 v[112:113], v[62:63], off offset:1536 nt
	v_add_u32_e32 v72, s21, v56
	s_mov_b32 s6, 0x8080
	v_cmp_gt_i32_e32 vcc, s6, v72
	s_mov_b64 s[6:7], 0
	s_mov_b64 s[8:9], 0
	v_mov_b32_e32 v58, v50
	s_and_saveexec_b64 s[16:17], vcc
	s_cbranch_execz .LBB0_1641
	s_mov_b32 s8, 0x7f807f81
	v_mul_hi_i32 v0, v72, s8
	v_lshrrev_b32_e32 v57, 31, v0
	v_ashrrev_i32_e32 v0, 11, v0
	v_add_u32_e32 v0, v0, v57
	v_mul_i32_i24_e32 v0, 0x1010, v0
	v_sub_u32_e32 v0, v72, v0
	v_readlane_b32 s8, v254, 52
	v_cmp_lt_i32_e32 vcc, 15, v0
	v_readlane_b32 s9, v254, 53
	s_or_b64 s[8:9], s[8:9], vcc
	s_and_b64 s[8:9], s[8:9], exec
	v_mov_b32_e32 v58, v72
.LBB0_1641:
	s_or_b64 exec, exec, s[16:17]
	s_add_i32 s20, s20, 1
	v_readlane_b32 s16, v51, s20
	v_readlane_b32 s18, v148, s20
	v_ashrrev_i32_e32 v59, 31, v58
	s_ashr_i32 s17, s16, 31
	v_lshlrev_b64 v[58:59], 11, v[58:59]
	s_lshl_b64 s[16:17], s[16:17], 11
	s_ashr_i32 s19, s18, 31
	v_lshl_add_u64 v[58:59], v[52:53], 0, v[58:59]
	v_lshl_add_u64 v[60:61], v[54:55], 0, s[16:17]
	s_lshl_b64 s[16:17], s[18:19], 11
	v_lshl_add_u64 v[62:63], v[54:55], 0, s[16:17]
	global_load_dwordx2 v[106:107], v[58:59], off nt
	global_load_dwordx2 v[100:101], v[58:59], off offset:512 nt
	global_load_dwordx2 v[92:93], v[58:59], off offset:1024 nt
	global_load_dwordx2 v[88:89], v[58:59], off offset:1536 nt
	global_load_dwordx2 v[110:111], v[60:61], off nt
	global_load_dwordx2 v[104:105], v[60:61], off offset:512 nt
	global_load_dwordx2 v[96:97], v[60:61], off offset:1024 nt
	global_load_dwordx2 v[90:91], v[60:61], off offset:1536 nt
	global_load_dwordx2 v[108:109], v[62:63], off nt
	global_load_dwordx2 v[102:103], v[62:63], off offset:512 nt
	global_load_dwordx2 v[94:95], v[62:63], off offset:1024 nt
	global_load_dwordx2 v[86:87], v[62:63], off offset:1536 nt
	s_mul_i32 s16, s76, 24
	v_add_u32_e32 v58, s16, v56
	s_mov_b32 s16, 0x8080
	v_cmp_gt_i32_e32 vcc, s16, v58
	v_mov_b32_e32 v60, v50
	s_and_saveexec_b64 s[16:17], vcc
	s_cbranch_execz .LBB0_1643
	s_mov_b32 s6, 0x7f807f81
	v_mul_hi_i32 v0, v58, s6
	v_lshrrev_b32_e32 v57, 31, v0
	v_ashrrev_i32_e32 v0, 11, v0
	v_add_u32_e32 v0, v0, v57
	v_mul_i32_i24_e32 v0, 0x1010, v0
	v_sub_u32_e32 v0, v58, v0
	v_readlane_b32 s6, v254, 52
	v_cmp_lt_i32_e32 vcc, 15, v0
	v_readlane_b32 s7, v254, 53
	s_or_b64 s[6:7], s[6:7], vcc
	s_and_b64 s[6:7], s[6:7], exec
	v_mov_b32_e32 v60, v58
; __device__ __forceinline__ float bflo(unsigned w) { return __uint_as_float(w << 16); }
; __device__ __forceinline__ float bfhi(unsigned w) { return __uint_as_float(w & 0xFFFF0000u); }
; __device__ __forceinline__ void ph_ln2(const Params& p, int l, LAS unsigned char* lds, const int wvid) {
;     ...
;     for (int r = gw; r < T; r += 4 * NGW, k += 4) {
;         u32x2 hv[4][4], av[4][4], cv[4][4]; bool on[4];
; #pragma unroll
;         for (int q = 0; q < 4; ++q) { const int rr = r + q * NGW; const int t = rr % LT; on[q] = rr < T && !(l == NLAYER - 1 && t < NMETA);
;             const int rc = rr < T ? rr : gw; const int s0 = __builtin_amdgcn_readlane(sl0, k + q), s1 = __builtin_amdgcn_readlane(sl1, k + q);
; #pragma unroll
;             for (int j = 0; j < 4; ++j) { hv[q][j] = *(const u32x2*)(HB + (size_t)rc * D + 4 * lane + 256 * j); av[q][j] = *(const u32x2*)(Y2 + (size_t)s0 * D + 4 * lane + 256 * j); cv[q][j] = *(const u32x2*)(Y2 + (size_t)s1 * D + 4 * lane + 256 * j); } }
; #pragma unroll
;         for (int q = 0; q < 4; ++q) { const int rr = r + q * NGW; if (!on[q]) continue; const int b = rr / LT, t = rr % LT;
;             f32x4 v[4];
; #pragma unroll
;             for (int j = 0; j < 4; ++j) { const u32x2 h = hv[q][j], a = av[q][j], c = cv[q][j];
;                 v[j][0] = ALPHA * bflo(h.x) + bflo(a.x) + bflo(c.x); v[j][1] = ALPHA * bfhi(h.x) + bfhi(a.x) + bfhi(c.x); v[j][2] = ALPHA * bflo(h.y) + bflo(a.y) + bflo(c.y); v[j][3] = ALPHA * bfhi(h.y) + bfhi(a.y) + bfhi(c.y); }
.LBB0_1643:
	s_or_b64 exec, exec, s[16:17]
	s_add_i32 s20, s20, 1
	v_readlane_b32 s16, v51, s20
	v_readlane_b32 s18, v148, s20
	v_ashrrev_i32_e32 v61, 31, v60
	s_ashr_i32 s17, s16, 31
	v_lshlrev_b64 v[60:61], 11, v[60:61]
	s_lshl_b64 s[16:17], s[16:17], 11
	s_ashr_i32 s19, s18, 31
	v_lshl_add_u64 v[60:61], v[52:53], 0, v[60:61]
	v_lshl_add_u64 v[64:65], v[54:55], 0, s[16:17]
	s_lshl_b64 s[16:17], s[18:19], 11
	v_lshl_add_u64 v[138:139], v[54:55], 0, s[16:17]
	global_load_dwordx2 v[80:81], v[60:61], off nt
	global_load_dwordx2 v[74:75], v[60:61], off offset:512 nt
	global_load_dwordx2 v[66:67], v[60:61], off offset:1024 nt
	global_load_dwordx2 v[62:63], v[60:61], off offset:1536 nt
	global_load_dwordx2 v[84:85], v[64:65], off nt
	global_load_dwordx2 v[78:79], v[64:65], off offset:512 nt
	global_load_dwordx2 v[70:71], v[64:65], off offset:1024 nt
	s_nop 0
	global_load_dwordx2 v[64:65], v[64:65], off offset:1536 nt
	s_nop 0
	global_load_dwordx2 v[82:83], v[138:139], off nt
	global_load_dwordx2 v[76:77], v[138:139], off offset:512 nt
	global_load_dwordx2 v[68:69], v[138:139], off offset:1024 nt
	global_load_dwordx2 v[60:61], v[138:139], off offset:1536 nt
	s_mov_b32 s16, 0x7f807f81
	v_mul_hi_i32 v0, v56, s16
	v_lshrrev_b32_e32 v57, 31, v0
	v_ashrrev_i32_e32 v0, 11, v0
	v_add_u32_e32 v138, v0, v57
	v_mul_i32_i24_e32 v0, 0x1010, v138
	v_sub_u32_e32 v0, v56, v0
	v_readlane_b32 s16, v254, 52
	v_cmp_lt_i32_e32 vcc, 15, v0
	v_readlane_b32 s17, v254, 53
	s_or_b64 s[18:19], s[16:17], vcc
	s_and_saveexec_b64 s[16:17], s[18:19]
	s_cbranch_execz .LBB0_1648
	s_waitcnt vmcnt(47)
	v_lshlrev_b32_e32 v150, 16, v142
	v_and_b32_e32 v151, 0xffff0000, v142
	s_waitcnt vmcnt(43)
	v_lshlrev_b32_e32 v152, 16, v146
	v_and_b32_e32 v153, 0xffff0000, v146
	v_lshlrev_b32_e32 v142, 16, v143
	v_and_b32_e32 v143, 0xffff0000, v143
	v_lshlrev_b32_e32 v146, 16, v147
	v_and_b32_e32 v147, 0xffff0000, v147
	v_pk_fma_f32 v[150:151], v[150:151], s[88:89], v[152:153] op_sel_hi:[1,0,1]
	s_waitcnt vmcnt(39)
	v_lshlrev_b32_e32 v152, 16, v144
	v_and_b32_e32 v153, 0xffff0000, v144
	v_pk_fma_f32 v[142:143], v[142:143], s[88:89], v[146:147] op_sel_hi:[1,0,1]
	v_lshlrev_b32_e32 v144, 16, v145
	v_and_b32_e32 v145, 0xffff0000, v145
	v_pk_add_f32 v[142:143], v[142:143], v[144:145]
	v_lshlrev_b32_e32 v144, 16, v46
	v_and_b32_e32 v145, 0xffff0000, v46
	v_lshlrev_b32_e32 v146, 16, v140
	v_and_b32_e32 v147, 0xffff0000, v140
	v_lshlrev_b32_e32 v46, 16, v47
	v_and_b32_e32 v47, 0xffff0000, v47
	v_lshlrev_b32_e32 v140, 16, v141
	v_and_b32_e32 v141, 0xffff0000, v141
	v_pk_fma_f32 v[144:145], v[144:145], s[88:89], v[146:147] op_sel_hi:[1,0,1]
	s_waitcnt vmcnt(38)
	v_lshlrev_b32_e32 v146, 16, v48
	v_and_b32_e32 v147, 0xffff0000, v48
	v_pk_fma_f32 v[46:47], v[46:47], s[88:89], v[140:141] op_sel_hi:[1,0,1]
	v_lshlrev_b32_e32 v48, 16, v49
	v_and_b32_e32 v49, 0xffff0000, v49
	v_pk_add_f32 v[140:141], v[46:47], v[48:49]
	v_lshlrev_b32_e32 v46, 16, v40
	v_and_b32_e32 v47, 0xffff0000, v40
	v_lshlrev_b32_e32 v48, 16, v44
	v_and_b32_e32 v49, 0xffff0000, v44
	v_lshlrev_b32_e32 v40, 16, v41
	v_and_b32_e32 v41, 0xffff0000, v41
	v_lshlrev_b32_e32 v44, 16, v45
	v_and_b32_e32 v45, 0xffff0000, v45
	v_pk_fma_f32 v[46:47], v[46:47], s[88:89], v[48:49] op_sel_hi:[1,0,1]
	s_waitcnt vmcnt(37)
	v_lshlrev_b32_e32 v48, 16, v42
	v_and_b32_e32 v49, 0xffff0000, v42
	v_pk_fma_f32 v[40:41], v[40:41], s[88:89], v[44:45] op_sel_hi:[1,0,1]
	v_lshlrev_b32_e32 v42, 16, v43
	v_and_b32_e32 v43, 0xffff0000, v43
	v_pk_add_f32 v[40:41], v[40:41], v[42:43]
	v_lshlrev_b32_e32 v42, 16, v36
	v_and_b32_e32 v43, 0xffff0000, v36
	v_lshlrev_b32_e32 v44, 16, v38
	v_and_b32_e32 v45, 0xffff0000, v38
	v_lshlrev_b32_e32 v36, 16, v37
	v_and_b32_e32 v37, 0xffff0000, v37
	v_lshlrev_b32_e32 v38, 16, v39
	v_and_b32_e32 v39, 0xffff0000, v39
	v_pk_add_f32 v[150:151], v[150:151], v[152:153]
	v_pk_fma_f32 v[42:43], v[42:43], s[88:89], v[44:45] op_sel_hi:[1,0,1]
	s_waitcnt vmcnt(36)
; __device__ __forceinline__ float bflo(unsigned w) { return __uint_as_float(w << 16); }
; __device__ __forceinline__ float bfhi(unsigned w) { return __uint_as_float(w & 0xFFFF0000u); }
; __device__ __forceinline__ float frsq(float x) { return __builtin_amdgcn_rsqf(x); }
; __device__ __forceinline__ void ln_affine(f32x4 (&v)[4], const LnPar& q) {
;     float s = 0.f;
; #pragma unroll
;     for (int j = 0; j < 4; ++j) s += (v[j][0] + v[j][1]) + (v[j][2] + v[j][3]);
;     const float mean = wave_sum(s) * (1.f / D); float s2 = 0.f;
; #pragma unroll
;     for (int j = 0; j < 4; ++j) { v[j] = v[j] - mean; s2 += (v[j][0] * v[j][0] + v[j][1] * v[j][1]) + (v[j][2] * v[j][2] + v[j][3] * v[j][3]); }
;     const float rstd = frsq(wave_sum(s2) * (1.f / D) + 1e-5f);
; #pragma unroll
;     for (int j = 0; j < 4; ++j) v[j] = v[j] * rstd * q.g[j] + q.b[j];
; }
; __device__ __forceinline__ void ph_ln2(const Params& p, int l, LAS unsigned char* lds, const int wvid) {
;     ...
;             for (int j = 0; j < 4; ++j) { const u32x2 h = hv[q][j], a = av[q][j], c = cv[q][j];
;                 v[j][0] = ALPHA * bflo(h.x) + bflo(a.x) + bflo(c.x); v[j][1] = ALPHA * bfhi(h.x) + bfhi(a.x) + bfhi(c.x); v[j][2] = ALPHA * bflo(h.y) + bflo(a.y) + bflo(c.y); v[j][3] = ALPHA * bfhi(h.y) + bfhi(a.y) + bfhi(c.y); }
;             ln_affine(v, ln2);
;             if (l == NLAYER - 1) { float* o = p.out + ((size_t)b * SEQ + (t - NMETA)) * D;
; #pragma unroll
;                 for (int j = 0; j < 4; ++j) *(f32x4*)(o + 4 * lane + 256 * j) = v[j]; }
	v_lshlrev_b32_e32 v44, 16, v34
	v_and_b32_e32 v45, 0xffff0000, v34
	v_pk_fma_f32 v[36:37], v[36:37], s[88:89], v[38:39] op_sel_hi:[1,0,1]
	v_lshlrev_b32_e32 v34, 16, v35
	v_and_b32_e32 v35, 0xffff0000, v35
	v_pk_add_f32 v[144:145], v[144:145], v[146:147]
	v_pk_add_f32 v[38:39], v[36:37], v[34:35]
	v_mov_b32_e32 v34, v150
	v_mov_b32_e32 v35, v142
	v_mov_b32_e32 v36, v151
	v_mov_b32_e32 v37, v143
	v_pk_add_f32 v[152:153], v[42:43], v[44:45]
	v_pk_add_f32 v[34:35], v[34:35], v[36:37]
	v_mov_b32_e32 v36, v144
	v_mov_b32_e32 v37, v140
	v_mov_b32_e32 v42, v145
	v_mov_b32_e32 v43, v141
	v_pk_add_f32 v[146:147], v[46:47], v[48:49]
	v_pk_add_f32 v[36:37], v[36:37], v[42:43]
	v_add_f32_e32 v34, v34, v35
	v_pk_add_f32 v[36:37], v[36:37], v[36:37] op_sel:[0,1] op_sel_hi:[1,0]
	v_pk_add_f32 v[42:43], v[146:147], v[146:147] op_sel:[0,1] op_sel_hi:[1,0]
	v_pk_add_f32 v[44:45], v[40:41], v[40:41] op_sel:[0,1] op_sel_hi:[1,0]
	v_add_f32_e32 v34, 0, v34
	v_mov_b32_e32 v35, v152
	v_mov_b32_e32 v37, v153
	v_mov_b32_e32 v43, v38
	v_mov_b32_e32 v45, v39
	v_pk_add_f32 v[34:35], v[34:35], v[36:37]
	v_pk_add_f32 v[36:37], v[42:43], v[44:45]
	s_nop 0
	v_pk_add_f32 v[34:35], v[34:35], v[36:37]
	s_nop 0
	v_add_f32_e32 v34, v34, v35
	v_mov_b32_e32 v35, v1
	s_nop 0
	v_add_f32_dpp v34, v34, v34 quad_perm:[1,0,3,2] row_mask:0xf bank_mask:0xf bound_ctrl:1
	s_nop 1
	v_add_f32_dpp v34, v34, v34 quad_perm:[2,3,0,1] row_mask:0xf bank_mask:0xf bound_ctrl:1
	s_nop 1
	v_add_f32_dpp v34, v34, v34 row_half_mirror row_mask:0xf bank_mask:0xf bound_ctrl:1
	s_nop 1
	v_add_f32_dpp v34, v34, v34 row_mirror row_mask:0xf bank_mask:0xf bound_ctrl:1
	s_nop 1
	v_mov_b32_dpp v35, v34 row_bcast:15 row_mask:0xa bank_mask:0xf
	v_add_f32_e32 v34, v34, v35
	v_mov_b32_e32 v35, v1
	s_nop 1
	v_mov_b32_dpp v35, v34 row_bcast:31 row_mask:0xc bank_mask:0xf
	v_add_f32_e32 v34, v34, v35
	s_nop 0
	v_readlane_b32 s18, v34, 63
	s_nop 1
	v_fma_f32 v151, s18, v220, v151
	v_fmac_f32_e32 v150, s18, v220
	v_fma_f32 v143, s18, v220, v143
	v_fmac_f32_e32 v142, s18, v220
	v_pk_mul_f32 v[34:35], v[142:143], v[142:143]
	v_pk_mul_f32 v[36:37], v[150:151], v[150:151]
	v_fma_f32 v145, s18, v220, v145
	v_pk_mov_b32 v[42:43], v[36:37], v[34:35] op_sel:[1,0]
	v_mov_b32_e32 v37, v35
	v_pk_add_f32 v[34:35], v[42:43], v[36:37]
	v_fmac_f32_e32 v144, s18, v220
	v_fma_f32 v141, s18, v220, v141
	v_fmac_f32_e32 v140, s18, v220
	v_pk_add_f32 v[34:35], v[34:35], v[34:35] op_sel_hi:[0,1]
	v_pk_mul_f32 v[36:37], v[140:141], v[140:141]
	v_pk_mul_f32 v[42:43], v[144:145], v[144:145]
	v_fmac_f32_e32 v146, s18, v220
	v_pk_mov_b32 v[44:45], v[42:43], v[36:37] op_sel:[1,0]
	v_mov_b32_e32 v43, v37
	v_fma_f32 v147, s18, v220, v147
	v_fmac_f32_e32 v40, s18, v220
	v_mul_f32_e32 v34, v146, v146
	v_pk_add_f32 v[36:37], v[44:45], v[42:43]
	v_fma_f32 v41, s18, v220, v41
	v_pk_fma_f32 v[42:43], v[146:147], v[146:147], v[34:35] op_sel_hi:[1,1,0]
	v_mul_f32_e32 v34, v40, v40
	v_pk_add_f32 v[36:37], v[36:37], v[36:37] op_sel_hi:[0,1]
	v_pk_fma_f32 v[44:45], v[40:41], v[40:41], v[34:35] op_sel_hi:[1,1,0]
	v_fma_f32 v39, s18, v220, v39
	v_fmac_f32_e32 v38, s18, v220
	v_fma_f32 v153, s18, v220, v153
	v_fmac_f32_e32 v152, s18, v220
	v_mul_f32_e32 v42, v152, v152
	v_mul_f32_e32 v44, v153, v153
	v_mul_f32_e32 v34, v38, v38
	v_mul_f32_e32 v36, v39, v39
	v_pk_add_f32 v[42:43], v[42:43], v[44:45]
	v_pk_add_f32 v[34:35], v[34:35], v[36:37]
	s_nop 0
	v_pk_add_f32 v[34:35], v[42:43], v[34:35]
	s_nop 0
	v_add_f32_e32 v34, v34, v35
	v_mov_b32_e32 v35, v1
	s_nop 0
	v_add_f32_dpp v34, v34, v34 quad_perm:[1,0,3,2] row_mask:0xf bank_mask:0xf bound_ctrl:1
	s_nop 1
	v_add_f32_dpp v34, v34, v34 quad_perm:[2,3,0,1] row_mask:0xf bank_mask:0xf bound_ctrl:1
	s_nop 1
	v_add_f32_dpp v34, v34, v34 row_half_mirror row_mask:0xf bank_mask:0xf bound_ctrl:1
	s_nop 1
	v_add_f32_dpp v34, v34, v34 row_mirror row_mask:0xf bank_mask:0xf bound_ctrl:1
	s_nop 1
	v_mov_b32_dpp v35, v34 row_bcast:15 row_mask:0xa bank_mask:0xf
	v_add_f32_e32 v34, v34, v35
	v_mov_b32_e32 v35, v1
	s_nop 1
	v_mov_b32_dpp v35, v34 row_bcast:31 row_mask:0xc bank_mask:0xf
	v_add_f32_e32 v34, v34, v35
	s_nop 0
	v_readlane_b32 s18, v34, 63
	s_nop 1
	v_fma_f32 v34, s18, v221, v204
	v_rsq_f32_e32 v154, v34
	v_readlane_b32 s18, v255, 10
	v_readlane_b32 s19, v255, 11
	s_andn2_b64 vcc, exec, s[18:19]
	v_pk_mul_f32 v[34:35], v[150:151], v[154:155] op_sel_hi:[1,0]
	v_pk_mul_f32 v[36:37], v[142:143], v[154:155] op_sel_hi:[1,0]
	v_pk_fma_f32 v[46:47], v[2:3], v[34:35], v[6:7]
	v_pk_fma_f32 v[48:49], v[4:5], v[36:37], v[8:9]
	v_pk_mul_f32 v[34:35], v[144:145], v[154:155] op_sel_hi:[1,0]
	v_pk_mul_f32 v[36:37], v[140:141], v[154:155] op_sel_hi:[1,0]
	v_pk_fma_f32 v[42:43], v[10:11], v[34:35], v[14:15]
	v_pk_fma_f32 v[44:45], v[12:13], v[36:37], v[16:17]
	v_pk_mul_f32 v[34:35], v[146:147], v[154:155] op_sel_hi:[1,0]
	v_pk_mul_f32 v[36:37], v[40:41], v[154:155] op_sel_hi:[1,0]
	v_pk_mul_f32 v[140:141], v[152:153], v[154:155] op_sel_hi:[1,0]
	v_pk_mul_f32 v[38:39], v[38:39], v[154:155] op_sel_hi:[1,0]
	v_pk_fma_f32 v[36:37], v[20:21], v[36:37], v[24:25]
	v_pk_fma_f32 v[34:35], v[18:19], v[34:35], v[22:23]
	v_pk_fma_f32 v[40:41], v[28:29], v[38:39], v[32:33]
	v_pk_fma_f32 v[38:39], v[26:27], v[140:141], v[30:31]
	s_mov_b64 s[18:19], -1
	s_cbranch_vccnz .LBB0_1646
	v_ashrrev_i32_e32 v139, 31, v138
	v_add_u32_e32 v140, -16, v0
	v_readlane_b32 s24, v253, 0
	v_ashrrev_i32_e32 v141, 31, v140
	v_lshlrev_b64 v[138:139], 24, v[138:139]
	v_readlane_b32 s26, v253, 2
	v_readlane_b32 s27, v253, 3
	v_lshlrev_b64 v[140:141], 12, v[140:141]
	v_lshlrev_b32_e32 v0, 2, v149
	v_lshl_add_u64 v[138:139], s[26:27], 0, v[138:139]
	v_lshl_add_u64 v[138:139], v[138:139], 0, v[140:141]
	v_lshl_add_u64 v[138:139], v[138:139], 0, v[0:1]
	s_mov_b64 s[18:19], 0
	v_readlane_b32 s25, v253, 1
	global_store_dwordx4 v[138:139], v[46:49], off nt
	global_store_dwordx4 v[138:139], v[42:45], off offset:1024 nt
	global_store_dwordx4 v[138:139], v[34:37], off offset:2048 nt
	global_store_dwordx4 v[138:139], v[38:41], off offset:3072 nt

; __device__ __forceinline__ float bflo(unsigned w) { return __uint_as_float(w << 16); }
; __device__ __forceinline__ float bfhi(unsigned w) { return __uint_as_float(w & 0xFFFF0000u); }
; __device__ __forceinline__ void ph_ln2(const Params& p, int l, LAS unsigned char* lds, const int wvid) {
;     ...
;         for (int q = 0; q < 4; ++q) { const int rr = r + q * NGW; if (!on[q]) continue; const int b = rr / LT, t = rr % LT;
;             f32x4 v[4];
; #pragma unroll
;             for (int j = 0; j < 4; ++j) { const u32x2 h = hv[q][j], a = av[q][j], c = cv[q][j];
;                 v[j][0] = ALPHA * bflo(h.x) + bflo(a.x) + bflo(c.x); v[j][1] = ALPHA * bfhi(h.x) + bfhi(a.x) + bfhi(c.x); v[j][2] = ALPHA * bflo(h.y) + bflo(a.y) + bflo(c.y); v[j][3] = ALPHA * bfhi(h.y) + bfhi(a.y) + bfhi(c.y); }
.LBB0_1648:
	s_or_b64 exec, exec, s[16:17]
	s_and_saveexec_b64 s[16:17], s[10:11]
	s_cbranch_execz .LBB0_1653
	s_waitcnt vmcnt(35)
	v_lshlrev_b32_e32 v34, 16, v132
	v_and_b32_e32 v35, 0xffff0000, v132
	s_waitcnt vmcnt(31)
	v_lshlrev_b32_e32 v36, 16, v136
	v_and_b32_e32 v37, 0xffff0000, v136
	v_pk_fma_f32 v[34:35], v[34:35], s[88:89], v[36:37] op_sel_hi:[1,0,1]
	s_waitcnt vmcnt(27)
	v_lshlrev_b32_e32 v36, 16, v134
	v_and_b32_e32 v37, 0xffff0000, v134
	v_pk_add_f32 v[34:35], v[34:35], v[36:37]
	v_lshlrev_b32_e32 v36, 16, v133
	v_and_b32_e32 v37, 0xffff0000, v133
	v_lshlrev_b32_e32 v38, 16, v137
	v_and_b32_e32 v39, 0xffff0000, v137
	v_pk_fma_f32 v[36:37], v[36:37], s[88:89], v[38:39] op_sel_hi:[1,0,1]
	v_lshlrev_b32_e32 v38, 16, v135
	v_and_b32_e32 v39, 0xffff0000, v135
	v_pk_add_f32 v[36:37], v[36:37], v[38:39]
	v_lshlrev_b32_e32 v38, 16, v126
	v_and_b32_e32 v39, 0xffff0000, v126
	v_lshlrev_b32_e32 v40, 16, v130
	v_and_b32_e32 v41, 0xffff0000, v130
	v_pk_fma_f32 v[38:39], v[38:39], s[88:89], v[40:41] op_sel_hi:[1,0,1]
	s_waitcnt vmcnt(26)
	v_lshlrev_b32_e32 v40, 16, v128
	v_and_b32_e32 v41, 0xffff0000, v128
	v_pk_add_f32 v[38:39], v[38:39], v[40:41]
	v_lshlrev_b32_e32 v40, 16, v127
	v_and_b32_e32 v41, 0xffff0000, v127
	v_lshlrev_b32_e32 v42, 16, v131
	v_and_b32_e32 v43, 0xffff0000, v131
	v_pk_fma_f32 v[40:41], v[40:41], s[88:89], v[42:43] op_sel_hi:[1,0,1]
	v_lshlrev_b32_e32 v42, 16, v129
	v_and_b32_e32 v43, 0xffff0000, v129
	v_pk_add_f32 v[40:41], v[40:41], v[42:43]
	v_lshlrev_b32_e32 v42, 16, v120
	v_and_b32_e32 v43, 0xffff0000, v120
	v_lshlrev_b32_e32 v44, 16, v124
	v_and_b32_e32 v45, 0xffff0000, v124
	v_pk_fma_f32 v[42:43], v[42:43], s[88:89], v[44:45] op_sel_hi:[1,0,1]
	s_waitcnt vmcnt(25)
	v_lshlrev_b32_e32 v44, 16, v122
	v_and_b32_e32 v45, 0xffff0000, v122
	v_pk_add_f32 v[118:119], v[42:43], v[44:45]
	v_lshlrev_b32_e32 v42, 16, v121
	v_and_b32_e32 v43, 0xffff0000, v121
	v_lshlrev_b32_e32 v44, 16, v125
	v_and_b32_e32 v45, 0xffff0000, v125
	v_pk_fma_f32 v[42:43], v[42:43], s[88:89], v[44:45] op_sel_hi:[1,0,1]
	v_lshlrev_b32_e32 v44, 16, v123
	v_and_b32_e32 v45, 0xffff0000, v123
	v_pk_add_f32 v[120:121], v[42:43], v[44:45]
	v_lshlrev_b32_e32 v42, 16, v114
	v_and_b32_e32 v43, 0xffff0000, v114
	v_lshlrev_b32_e32 v44, 16, v116
	v_and_b32_e32 v45, 0xffff0000, v116
	v_pk_fma_f32 v[42:43], v[42:43], s[88:89], v[44:45] op_sel_hi:[1,0,1]
	s_waitcnt vmcnt(24)
; __device__ __forceinline__ float bflo(unsigned w) { return __uint_as_float(w << 16); }
; __device__ __forceinline__ float bfhi(unsigned w) { return __uint_as_float(w & 0xFFFF0000u); }
; __device__ __forceinline__ float frsq(float x) { return __builtin_amdgcn_rsqf(x); }
; __device__ __forceinline__ void ln_affine(f32x4 (&v)[4], const LnPar& q) {
;     float s = 0.f;
; #pragma unroll
;     for (int j = 0; j < 4; ++j) s += (v[j][0] + v[j][1]) + (v[j][2] + v[j][3]);
;     const float mean = wave_sum(s) * (1.f / D); float s2 = 0.f;
; #pragma unroll
;     for (int j = 0; j < 4; ++j) { v[j] = v[j] - mean; s2 += (v[j][0] * v[j][0] + v[j][1] * v[j][1]) + (v[j][2] * v[j][2] + v[j][3] * v[j][3]); }
;     const float rstd = frsq(wave_sum(s2) * (1.f / D) + 1e-5f);
; #pragma unroll
;     for (int j = 0; j < 4; ++j) v[j] = v[j] * rstd * q.g[j] + q.b[j];
; }
; __device__ __forceinline__ void ph_ln2(const Params& p, int l, LAS unsigned char* lds, const int wvid) {
;     ...
;             for (int j = 0; j < 4; ++j) { const u32x2 h = hv[q][j], a = av[q][j], c = cv[q][j];
;                 v[j][0] = ALPHA * bflo(h.x) + bflo(a.x) + bflo(c.x); v[j][1] = ALPHA * bfhi(h.x) + bfhi(a.x) + bfhi(c.x); v[j][2] = ALPHA * bflo(h.y) + bflo(a.y) + bflo(c.y); v[j][3] = ALPHA * bfhi(h.y) + bfhi(a.y) + bfhi(c.y); }
;             ln_affine(v, ln2);
;             if (l == NLAYER - 1) { float* o = p.out + ((size_t)b * SEQ + (t - NMETA)) * D;
; #pragma unroll
;                 for (int j = 0; j < 4; ++j) *(f32x4*)(o + 4 * lane + 256 * j) = v[j]; }
	v_lshlrev_b32_e32 v44, 16, v112
	v_and_b32_e32 v45, 0xffff0000, v112
	v_pk_add_f32 v[122:123], v[42:43], v[44:45]
	v_lshlrev_b32_e32 v42, 16, v115
	v_and_b32_e32 v43, 0xffff0000, v115
	v_lshlrev_b32_e32 v44, 16, v117
	v_and_b32_e32 v45, 0xffff0000, v117
	v_pk_fma_f32 v[42:43], v[42:43], s[88:89], v[44:45] op_sel_hi:[1,0,1]
	v_lshlrev_b32_e32 v44, 16, v113
	v_and_b32_e32 v45, 0xffff0000, v113
	v_pk_add_f32 v[112:113], v[42:43], v[44:45]
	v_mov_b32_e32 v42, v34
	v_mov_b32_e32 v43, v36
	v_mov_b32_e32 v44, v35
	v_mov_b32_e32 v45, v37
	v_pk_add_f32 v[42:43], v[42:43], v[44:45]
	v_mov_b32_e32 v44, v38
	v_mov_b32_e32 v45, v40
	v_mov_b32_e32 v46, v39
	v_mov_b32_e32 v47, v41
	v_pk_add_f32 v[44:45], v[44:45], v[46:47]
	v_add_f32_e32 v0, v42, v43
	v_pk_add_f32 v[44:45], v[44:45], v[44:45] op_sel:[0,1] op_sel_hi:[1,0]
	v_pk_add_f32 v[46:47], v[118:119], v[118:119] op_sel:[0,1] op_sel_hi:[1,0]
	v_pk_add_f32 v[48:49], v[120:121], v[120:121] op_sel:[0,1] op_sel_hi:[1,0]
	v_add_f32_e32 v42, 0, v0
	v_mov_b32_e32 v43, v122
	v_mov_b32_e32 v45, v123
	v_mov_b32_e32 v47, v112
	v_mov_b32_e32 v49, v113
	v_pk_add_f32 v[42:43], v[42:43], v[44:45]
	v_pk_add_f32 v[44:45], v[46:47], v[48:49]
	s_nop 0
	v_pk_add_f32 v[42:43], v[42:43], v[44:45]
	s_nop 0
	v_add_f32_e32 v0, v42, v43
	v_mov_b32_e32 v42, v1
	s_nop 0
	v_add_f32_dpp v0, v0, v0 quad_perm:[1,0,3,2] row_mask:0xf bank_mask:0xf bound_ctrl:1
	s_nop 1
	v_add_f32_dpp v0, v0, v0 quad_perm:[2,3,0,1] row_mask:0xf bank_mask:0xf bound_ctrl:1
	s_nop 1
	v_add_f32_dpp v0, v0, v0 row_half_mirror row_mask:0xf bank_mask:0xf bound_ctrl:1
	s_nop 1
	v_add_f32_dpp v0, v0, v0 row_mirror row_mask:0xf bank_mask:0xf bound_ctrl:1
	s_nop 1
	v_mov_b32_dpp v42, v0 row_bcast:15 row_mask:0xa bank_mask:0xf
	v_add_f32_e32 v0, v0, v42
	v_mov_b32_e32 v42, v1
	s_nop 1
	v_mov_b32_dpp v42, v0 row_bcast:31 row_mask:0xc bank_mask:0xf
	v_add_f32_e32 v0, v0, v42
	s_nop 0
	v_readlane_b32 s10, v0, 63
	s_nop 1
	v_fma_f32 v35, s10, v220, v35
	v_fmac_f32_e32 v34, s10, v220
	v_fma_f32 v37, s10, v220, v37
	v_fmac_f32_e32 v36, s10, v220
	v_pk_mul_f32 v[42:43], v[36:37], v[36:37]
	v_pk_mul_f32 v[44:45], v[34:35], v[34:35]
	v_fma_f32 v39, s10, v220, v39
	v_pk_mov_b32 v[46:47], v[44:45], v[42:43] op_sel:[1,0]
	v_mov_b32_e32 v45, v43
	v_fmac_f32_e32 v38, s10, v220
	v_fma_f32 v41, s10, v220, v41
	v_fmac_f32_e32 v40, s10, v220
	v_pk_add_f32 v[42:43], v[46:47], v[44:45]
	v_pk_mul_f32 v[44:45], v[40:41], v[40:41]
	v_pk_mul_f32 v[46:47], v[38:39], v[38:39]
	v_fmac_f32_e32 v118, s10, v220
	v_pk_mov_b32 v[48:49], v[46:47], v[44:45] op_sel:[1,0]
	v_mov_b32_e32 v47, v45
	v_fma_f32 v119, s10, v220, v119
	v_fmac_f32_e32 v120, s10, v220
	v_mul_f32_e32 v0, v118, v118
	v_pk_add_f32 v[44:45], v[48:49], v[46:47]
	v_fma_f32 v121, s10, v220, v121
	v_pk_fma_f32 v[46:47], v[118:119], v[118:119], v[0:1] op_sel_hi:[1,1,0]
	v_mul_f32_e32 v0, v120, v120
	v_pk_add_f32 v[42:43], v[42:43], v[42:43] op_sel_hi:[0,1]
	v_pk_add_f32 v[44:45], v[44:45], v[44:45] op_sel_hi:[0,1]
	v_pk_fma_f32 v[48:49], v[120:121], v[120:121], v[0:1] op_sel_hi:[1,1,0]
	v_fma_f32 v113, s10, v220, v113
	v_fmac_f32_e32 v112, s10, v220
	v_fma_f32 v123, s10, v220, v123
	v_fmac_f32_e32 v122, s10, v220
	v_mul_f32_e32 v46, v122, v122
	v_mul_f32_e32 v48, v123, v123
	v_mul_f32_e32 v42, v112, v112
	v_mul_f32_e32 v44, v113, v113
	v_pk_add_f32 v[46:47], v[46:47], v[48:49]
	v_pk_add_f32 v[42:43], v[42:43], v[44:45]
	s_nop 0
	v_pk_add_f32 v[42:43], v[46:47], v[42:43]
	s_nop 0
	v_add_f32_e32 v0, v42, v43
	v_mov_b32_e32 v42, v1
	s_nop 0
	v_add_f32_dpp v0, v0, v0 quad_perm:[1,0,3,2] row_mask:0xf bank_mask:0xf bound_ctrl:1
	s_nop 1
	v_add_f32_dpp v0, v0, v0 quad_perm:[2,3,0,1] row_mask:0xf bank_mask:0xf bound_ctrl:1
	s_nop 1
	v_add_f32_dpp v0, v0, v0 row_half_mirror row_mask:0xf bank_mask:0xf bound_ctrl:1
	s_nop 1
	v_add_f32_dpp v0, v0, v0 row_mirror row_mask:0xf bank_mask:0xf bound_ctrl:1
	s_nop 1
	v_mov_b32_dpp v42, v0 row_bcast:15 row_mask:0xa bank_mask:0xf
	v_add_f32_e32 v0, v0, v42
	v_mov_b32_e32 v42, v1
	s_nop 1
	v_mov_b32_dpp v42, v0 row_bcast:31 row_mask:0xc bank_mask:0xf
	v_add_f32_e32 v0, v0, v42
	s_nop 0
	v_readlane_b32 s10, v0, 63
	s_nop 1
	v_fma_f32 v0, s10, v221, v204
	v_rsq_f32_e32 v0, v0
	v_readlane_b32 s10, v255, 10
	v_readlane_b32 s11, v255, 11
	s_andn2_b64 vcc, exec, s[10:11]
	v_pk_mul_f32 v[34:35], v[34:35], v[0:1] op_sel_hi:[1,0]
	v_pk_mul_f32 v[36:37], v[36:37], v[0:1] op_sel_hi:[1,0]
	v_pk_fma_f32 v[46:47], v[2:3], v[34:35], v[6:7]
	v_pk_fma_f32 v[48:49], v[4:5], v[36:37], v[8:9]
	v_pk_mul_f32 v[34:35], v[38:39], v[0:1] op_sel_hi:[1,0]
	v_pk_mul_f32 v[36:37], v[40:41], v[0:1] op_sel_hi:[1,0]
	v_pk_fma_f32 v[42:43], v[10:11], v[34:35], v[14:15]
	v_pk_fma_f32 v[44:45], v[12:13], v[36:37], v[16:17]
	v_pk_mul_f32 v[34:35], v[118:119], v[0:1] op_sel_hi:[1,0]
	v_pk_mul_f32 v[36:37], v[120:121], v[0:1] op_sel_hi:[1,0]
	v_pk_mul_f32 v[38:39], v[122:123], v[0:1] op_sel_hi:[1,0]
	v_pk_mul_f32 v[40:41], v[112:113], v[0:1] op_sel_hi:[1,0]
	v_pk_fma_f32 v[36:37], v[20:21], v[36:37], v[24:25]
	v_pk_fma_f32 v[34:35], v[18:19], v[34:35], v[22:23]
	v_pk_fma_f32 v[40:41], v[28:29], v[40:41], v[32:33]
	v_pk_fma_f32 v[38:39], v[26:27], v[38:39], v[30:31]
	s_mov_b64 s[10:11], -1
	s_cbranch_vccnz .LBB0_1651
	s_mov_b32 s10, 0x7f807f81
	v_mul_hi_i32 v0, v98, s10
	v_lshrrev_b32_e32 v57, 31, v0
	v_ashrrev_i32_e32 v0, 11, v0
	v_add_u32_e32 v112, v0, v57
	v_mul_i32_i24_e32 v0, 0x1010, v112
	v_sub_u32_e32 v114, v98, v0
	v_ashrrev_i32_e32 v113, 31, v112
	v_readlane_b32 s24, v253, 0
	v_ashrrev_i32_e32 v115, 31, v114
	v_lshlrev_b64 v[112:113], 24, v[112:113]
	v_readlane_b32 s26, v253, 2
	v_readlane_b32 s27, v253, 3
	v_lshlrev_b64 v[114:115], 12, v[114:115]
	v_lshlrev_b32_e32 v0, 2, v149
	v_lshl_add_u64 v[112:113], s[26:27], 0, v[112:113]
	v_lshl_add_u64 v[112:113], v[112:113], 0, v[114:115]
	s_mov_b32 s10, 0xffff0000
	v_lshl_add_u64 v[112:113], v[112:113], 0, v[0:1]
	s_mov_b32 s11, -1
	v_lshl_add_u64 v[114:115], v[112:113], 0, s[10:11]
	v_add_co_u32_e32 v112, vcc, 0xffff0000, v112
	s_mov_b64 s[10:11], 0
	s_nop 0
	v_addc_co_u32_e32 v113, vcc, -1, v113, vcc
	v_readlane_b32 s25, v253, 1
	global_store_dwordx4 v[112:113], v[46:49], off nt
	global_store_dwordx4 v[114:115], v[42:45], off offset:1024 nt
	global_store_dwordx4 v[114:115], v[34:37], off offset:2048 nt
	global_store_dwordx4 v[114:115], v[38:41], off offset:3072 nt

; __device__ __forceinline__ float bflo(unsigned w) { return __uint_as_float(w << 16); }
; __device__ __forceinline__ float bfhi(unsigned w) { return __uint_as_float(w & 0xFFFF0000u); }
; __device__ __forceinline__ void ph_ln2(const Params& p, int l, LAS unsigned char* lds, const int wvid) {
;     ...
;         for (int q = 0; q < 4; ++q) { const int rr = r + q * NGW; if (!on[q]) continue; const int b = rr / LT, t = rr % LT;
;             f32x4 v[4];
; #pragma unroll
;             for (int j = 0; j < 4; ++j) { const u32x2 h = hv[q][j], a = av[q][j], c = cv[q][j];
;                 v[j][0] = ALPHA * bflo(h.x) + bflo(a.x) + bflo(c.x); v[j][1] = ALPHA * bfhi(h.x) + bfhi(a.x) + bfhi(c.x); v[j][2] = ALPHA * bflo(h.y) + bflo(a.y) + bflo(c.y); v[j][3] = ALPHA * bfhi(h.y) + bfhi(a.y) + bfhi(c.y); }
.LBB0_1653:
	s_or_b64 exec, exec, s[16:17]
	s_and_saveexec_b64 s[10:11], s[8:9]
	s_cbranch_execz .LBB0_1658
	s_waitcnt vmcnt(23)
	v_lshlrev_b32_e32 v34, 16, v106
	v_and_b32_e32 v35, 0xffff0000, v106
	s_waitcnt vmcnt(19)
	v_lshlrev_b32_e32 v36, 16, v110
	v_and_b32_e32 v37, 0xffff0000, v110
	v_pk_fma_f32 v[34:35], v[34:35], s[88:89], v[36:37] op_sel_hi:[1,0,1]
	s_waitcnt vmcnt(15)
	v_lshlrev_b32_e32 v36, 16, v108
	v_and_b32_e32 v37, 0xffff0000, v108
	v_pk_add_f32 v[34:35], v[34:35], v[36:37]
	v_lshlrev_b32_e32 v36, 16, v107
	v_and_b32_e32 v37, 0xffff0000, v107
	v_lshlrev_b32_e32 v38, 16, v111
	v_and_b32_e32 v39, 0xffff0000, v111
	v_pk_fma_f32 v[36:37], v[36:37], s[88:89], v[38:39] op_sel_hi:[1,0,1]
	v_lshlrev_b32_e32 v38, 16, v109
	v_and_b32_e32 v39, 0xffff0000, v109
	v_pk_add_f32 v[36:37], v[36:37], v[38:39]
	v_lshlrev_b32_e32 v38, 16, v100
	v_and_b32_e32 v39, 0xffff0000, v100
	v_lshlrev_b32_e32 v40, 16, v104
	v_and_b32_e32 v41, 0xffff0000, v104
	v_pk_fma_f32 v[38:39], v[38:39], s[88:89], v[40:41] op_sel_hi:[1,0,1]
	s_waitcnt vmcnt(14)
	v_lshlrev_b32_e32 v40, 16, v102
	v_and_b32_e32 v41, 0xffff0000, v102
	v_pk_add_f32 v[38:39], v[38:39], v[40:41]
	v_lshlrev_b32_e32 v40, 16, v101
	v_and_b32_e32 v41, 0xffff0000, v101
	v_lshlrev_b32_e32 v42, 16, v105
	v_and_b32_e32 v43, 0xffff0000, v105
	v_pk_fma_f32 v[40:41], v[40:41], s[88:89], v[42:43] op_sel_hi:[1,0,1]
	v_lshlrev_b32_e32 v42, 16, v103
	v_and_b32_e32 v43, 0xffff0000, v103
	v_pk_add_f32 v[40:41], v[40:41], v[42:43]
	v_lshlrev_b32_e32 v42, 16, v92
	v_and_b32_e32 v43, 0xffff0000, v92
	v_lshlrev_b32_e32 v44, 16, v96
	v_and_b32_e32 v45, 0xffff0000, v96
	v_pk_fma_f32 v[42:43], v[42:43], s[88:89], v[44:45] op_sel_hi:[1,0,1]
	s_waitcnt vmcnt(13)
	v_lshlrev_b32_e32 v44, 16, v94
	v_and_b32_e32 v45, 0xffff0000, v94
	v_pk_add_f32 v[98:99], v[42:43], v[44:45]
	v_lshlrev_b32_e32 v42, 16, v93
	v_and_b32_e32 v43, 0xffff0000, v93
	v_lshlrev_b32_e32 v44, 16, v97
	v_and_b32_e32 v45, 0xffff0000, v97
	v_pk_fma_f32 v[42:43], v[42:43], s[88:89], v[44:45] op_sel_hi:[1,0,1]
	v_lshlrev_b32_e32 v44, 16, v95
	v_and_b32_e32 v45, 0xffff0000, v95
	v_pk_add_f32 v[92:93], v[42:43], v[44:45]
	v_lshlrev_b32_e32 v42, 16, v88
	v_and_b32_e32 v43, 0xffff0000, v88
	v_lshlrev_b32_e32 v44, 16, v90
	v_and_b32_e32 v45, 0xffff0000, v90
	v_pk_fma_f32 v[42:43], v[42:43], s[88:89], v[44:45] op_sel_hi:[1,0,1]
	s_waitcnt vmcnt(12)
; __device__ __forceinline__ float bflo(unsigned w) { return __uint_as_float(w << 16); }
; __device__ __forceinline__ float bfhi(unsigned w) { return __uint_as_float(w & 0xFFFF0000u); }
; __device__ __forceinline__ float frsq(float x) { return __builtin_amdgcn_rsqf(x); }
; __device__ __forceinline__ void ln_affine(f32x4 (&v)[4], const LnPar& q) {
;     float s = 0.f;
; #pragma unroll
;     for (int j = 0; j < 4; ++j) s += (v[j][0] + v[j][1]) + (v[j][2] + v[j][3]);
;     const float mean = wave_sum(s) * (1.f / D); float s2 = 0.f;
; #pragma unroll
;     for (int j = 0; j < 4; ++j) { v[j] = v[j] - mean; s2 += (v[j][0] * v[j][0] + v[j][1] * v[j][1]) + (v[j][2] * v[j][2] + v[j][3] * v[j][3]); }
;     const float rstd = frsq(wave_sum(s2) * (1.f / D) + 1e-5f);
; #pragma unroll
;     for (int j = 0; j < 4; ++j) v[j] = v[j] * rstd * q.g[j] + q.b[j];
; }
; __device__ __forceinline__ void ph_ln2(const Params& p, int l, LAS unsigned char* lds, const int wvid) {
;     ...
;                 v[j][0] = ALPHA * bflo(h.x) + bflo(a.x) + bflo(c.x); v[j][1] = ALPHA * bfhi(h.x) + bfhi(a.x) + bfhi(c.x); v[j][2] = ALPHA * bflo(h.y) + bflo(a.y) + bflo(c.y); v[j][3] = ALPHA * bfhi(h.y) + bfhi(a.y) + bfhi(c.y); }
;             ln_affine(v, ln2);
;             if (l == NLAYER - 1) { float* o = p.out + ((size_t)b * SEQ + (t - NMETA)) * D;
; #pragma unroll
;                 for (int j = 0; j < 4; ++j) *(f32x4*)(o + 4 * lane + 256 * j) = v[j]; }
	v_lshlrev_b32_e32 v44, 16, v86
	v_and_b32_e32 v45, 0xffff0000, v86
	v_pk_add_f32 v[94:95], v[42:43], v[44:45]
	v_lshlrev_b32_e32 v42, 16, v89
	v_and_b32_e32 v43, 0xffff0000, v89
	v_lshlrev_b32_e32 v44, 16, v91
	v_and_b32_e32 v45, 0xffff0000, v91
	v_pk_fma_f32 v[42:43], v[42:43], s[88:89], v[44:45] op_sel_hi:[1,0,1]
	v_lshlrev_b32_e32 v44, 16, v87
	v_and_b32_e32 v45, 0xffff0000, v87
	v_pk_add_f32 v[86:87], v[42:43], v[44:45]
	v_mov_b32_e32 v42, v34
	v_mov_b32_e32 v43, v36
	v_mov_b32_e32 v44, v35
	v_mov_b32_e32 v45, v37
	v_pk_add_f32 v[42:43], v[42:43], v[44:45]
	v_mov_b32_e32 v44, v38
	v_mov_b32_e32 v45, v40
	v_mov_b32_e32 v46, v39
	v_mov_b32_e32 v47, v41
	v_pk_add_f32 v[44:45], v[44:45], v[46:47]
	v_add_f32_e32 v0, v42, v43
	v_pk_add_f32 v[44:45], v[44:45], v[44:45] op_sel:[0,1] op_sel_hi:[1,0]
	v_pk_add_f32 v[46:47], v[98:99], v[98:99] op_sel:[0,1] op_sel_hi:[1,0]
	v_pk_add_f32 v[48:49], v[92:93], v[92:93] op_sel:[0,1] op_sel_hi:[1,0]
	v_add_f32_e32 v42, 0, v0
	v_mov_b32_e32 v43, v94
	v_mov_b32_e32 v45, v95
	v_mov_b32_e32 v47, v86
	v_mov_b32_e32 v49, v87
	v_pk_add_f32 v[42:43], v[42:43], v[44:45]
	v_pk_add_f32 v[44:45], v[46:47], v[48:49]
	s_nop 0
	v_pk_add_f32 v[42:43], v[42:43], v[44:45]
	s_nop 0
	v_add_f32_e32 v0, v42, v43
	v_mov_b32_e32 v42, v1
	s_nop 0
	v_add_f32_dpp v0, v0, v0 quad_perm:[1,0,3,2] row_mask:0xf bank_mask:0xf bound_ctrl:1
	s_nop 1
	v_add_f32_dpp v0, v0, v0 quad_perm:[2,3,0,1] row_mask:0xf bank_mask:0xf bound_ctrl:1
	s_nop 1
	v_add_f32_dpp v0, v0, v0 row_half_mirror row_mask:0xf bank_mask:0xf bound_ctrl:1
	s_nop 1
	v_add_f32_dpp v0, v0, v0 row_mirror row_mask:0xf bank_mask:0xf bound_ctrl:1
	s_nop 1
	v_mov_b32_dpp v42, v0 row_bcast:15 row_mask:0xa bank_mask:0xf
	v_add_f32_e32 v0, v0, v42
	v_mov_b32_e32 v42, v1
	s_nop 1
	v_mov_b32_dpp v42, v0 row_bcast:31 row_mask:0xc bank_mask:0xf
	v_add_f32_e32 v0, v0, v42
	s_nop 0
	v_readlane_b32 s8, v0, 63
	s_nop 1
	v_fma_f32 v35, s8, v220, v35
	v_fmac_f32_e32 v34, s8, v220
	v_fma_f32 v37, s8, v220, v37
	v_fmac_f32_e32 v36, s8, v220
	v_pk_mul_f32 v[42:43], v[36:37], v[36:37]
	v_pk_mul_f32 v[44:45], v[34:35], v[34:35]
	v_fma_f32 v39, s8, v220, v39
	v_pk_mov_b32 v[46:47], v[44:45], v[42:43] op_sel:[1,0]
	v_mov_b32_e32 v45, v43
	v_fmac_f32_e32 v38, s8, v220
	v_fma_f32 v41, s8, v220, v41
	v_fmac_f32_e32 v40, s8, v220
	v_pk_add_f32 v[42:43], v[46:47], v[44:45]
	v_pk_mul_f32 v[44:45], v[40:41], v[40:41]
	v_pk_mul_f32 v[46:47], v[38:39], v[38:39]
	v_fmac_f32_e32 v98, s8, v220
	v_pk_mov_b32 v[48:49], v[46:47], v[44:45] op_sel:[1,0]
	v_mov_b32_e32 v47, v45
	v_fma_f32 v99, s8, v220, v99
	v_fmac_f32_e32 v92, s8, v220
	v_mul_f32_e32 v0, v98, v98
	v_pk_add_f32 v[44:45], v[48:49], v[46:47]
	v_fma_f32 v93, s8, v220, v93
	v_pk_fma_f32 v[46:47], v[98:99], v[98:99], v[0:1] op_sel_hi:[1,1,0]
	v_mul_f32_e32 v0, v92, v92
	v_pk_add_f32 v[42:43], v[42:43], v[42:43] op_sel_hi:[0,1]
	v_pk_add_f32 v[44:45], v[44:45], v[44:45] op_sel_hi:[0,1]
	v_pk_fma_f32 v[48:49], v[92:93], v[92:93], v[0:1] op_sel_hi:[1,1,0]
	v_fma_f32 v87, s8, v220, v87
	v_fmac_f32_e32 v86, s8, v220
	v_fma_f32 v95, s8, v220, v95
	v_fmac_f32_e32 v94, s8, v220
	v_mul_f32_e32 v46, v94, v94
	v_mul_f32_e32 v48, v95, v95
	v_mul_f32_e32 v42, v86, v86
	v_mul_f32_e32 v44, v87, v87
	v_pk_add_f32 v[46:47], v[46:47], v[48:49]
	v_pk_add_f32 v[42:43], v[42:43], v[44:45]
	s_nop 0
	v_pk_add_f32 v[42:43], v[46:47], v[42:43]
	s_nop 0
	v_add_f32_e32 v0, v42, v43
	v_mov_b32_e32 v42, v1
	s_nop 0
	v_add_f32_dpp v0, v0, v0 quad_perm:[1,0,3,2] row_mask:0xf bank_mask:0xf bound_ctrl:1
	s_nop 1
	v_add_f32_dpp v0, v0, v0 quad_perm:[2,3,0,1] row_mask:0xf bank_mask:0xf bound_ctrl:1
	s_nop 1
	v_add_f32_dpp v0, v0, v0 row_half_mirror row_mask:0xf bank_mask:0xf bound_ctrl:1
	s_nop 1
	v_add_f32_dpp v0, v0, v0 row_mirror row_mask:0xf bank_mask:0xf bound_ctrl:1
	s_nop 1
	v_mov_b32_dpp v42, v0 row_bcast:15 row_mask:0xa bank_mask:0xf
	v_add_f32_e32 v0, v0, v42
	v_mov_b32_e32 v42, v1
	s_nop 1
	v_mov_b32_dpp v42, v0 row_bcast:31 row_mask:0xc bank_mask:0xf
	v_add_f32_e32 v0, v0, v42
	s_nop 0
	v_readlane_b32 s8, v0, 63
	s_nop 1
	v_fma_f32 v0, s8, v221, v204
	v_rsq_f32_e32 v0, v0
	v_readlane_b32 s8, v255, 10
	v_readlane_b32 s9, v255, 11
	s_andn2_b64 vcc, exec, s[8:9]
	v_pk_mul_f32 v[34:35], v[34:35], v[0:1] op_sel_hi:[1,0]
	v_pk_mul_f32 v[36:37], v[36:37], v[0:1] op_sel_hi:[1,0]
	v_pk_fma_f32 v[46:47], v[2:3], v[34:35], v[6:7]
	v_pk_fma_f32 v[48:49], v[4:5], v[36:37], v[8:9]
	v_pk_mul_f32 v[34:35], v[38:39], v[0:1] op_sel_hi:[1,0]
	v_pk_mul_f32 v[36:37], v[40:41], v[0:1] op_sel_hi:[1,0]
	v_pk_fma_f32 v[42:43], v[10:11], v[34:35], v[14:15]
	v_pk_fma_f32 v[44:45], v[12:13], v[36:37], v[16:17]
	v_pk_mul_f32 v[34:35], v[98:99], v[0:1] op_sel_hi:[1,0]
	v_pk_mul_f32 v[36:37], v[92:93], v[0:1] op_sel_hi:[1,0]
	v_pk_mul_f32 v[38:39], v[94:95], v[0:1] op_sel_hi:[1,0]
	v_pk_mul_f32 v[40:41], v[86:87], v[0:1] op_sel_hi:[1,0]
	v_pk_fma_f32 v[36:37], v[20:21], v[36:37], v[24:25]
	v_pk_fma_f32 v[34:35], v[18:19], v[34:35], v[22:23]
	v_pk_fma_f32 v[40:41], v[28:29], v[40:41], v[32:33]
	v_pk_fma_f32 v[38:39], v[26:27], v[38:39], v[30:31]
	s_mov_b64 s[8:9], -1
	s_cbranch_vccnz .LBB0_1656
	s_mov_b32 s8, 0x7f807f81
	v_mul_hi_i32 v0, v72, s8
	v_lshrrev_b32_e32 v57, 31, v0
	v_ashrrev_i32_e32 v0, 11, v0
	v_add_u32_e32 v86, v0, v57
	v_mul_i32_i24_e32 v0, 0x1010, v86
	v_sub_u32_e32 v88, v72, v0
	v_ashrrev_i32_e32 v87, 31, v86
	v_readlane_b32 s16, v253, 0
	v_ashrrev_i32_e32 v89, 31, v88
	v_lshlrev_b64 v[86:87], 24, v[86:87]
	v_readlane_b32 s18, v253, 2
	v_readlane_b32 s19, v253, 3
	v_lshlrev_b64 v[88:89], 12, v[88:89]
	v_lshlrev_b32_e32 v0, 2, v149
	v_lshl_add_u64 v[86:87], s[18:19], 0, v[86:87]
	v_lshl_add_u64 v[86:87], v[86:87], 0, v[88:89]
	s_mov_b32 s8, 0xffff0000
	v_lshl_add_u64 v[86:87], v[86:87], 0, v[0:1]
	s_mov_b32 s9, -1
	v_lshl_add_u64 v[88:89], v[86:87], 0, s[8:9]
	v_add_co_u32_e32 v86, vcc, 0xffff0000, v86
	s_mov_b64 s[8:9], 0
	s_nop 0
	v_addc_co_u32_e32 v87, vcc, -1, v87, vcc
	v_readlane_b32 s17, v253, 1
	global_store_dwordx4 v[86:87], v[46:49], off nt
	global_store_dwordx4 v[88:89], v[42:45], off offset:1024 nt
	global_store_dwordx4 v[88:89], v[34:37], off offset:2048 nt
	global_store_dwordx4 v[88:89], v[38:41], off offset:3072 nt

; __device__ __forceinline__ float bflo(unsigned w) { return __uint_as_float(w << 16); }
; __device__ __forceinline__ float bfhi(unsigned w) { return __uint_as_float(w & 0xFFFF0000u); }
; __device__ __forceinline__ void ph_ln2(const Params& p, int l, LAS unsigned char* lds, const int wvid) {
;     ...
;         for (int q = 0; q < 4; ++q) { const int rr = r + q * NGW; if (!on[q]) continue; const int b = rr / LT, t = rr % LT;
;             f32x4 v[4];
; #pragma unroll
;             for (int j = 0; j < 4; ++j) { const u32x2 h = hv[q][j], a = av[q][j], c = cv[q][j];
;                 v[j][0] = ALPHA * bflo(h.x) + bflo(a.x) + bflo(c.x); v[j][1] = ALPHA * bfhi(h.x) + bfhi(a.x) + bfhi(c.x); v[j][2] = ALPHA * bflo(h.y) + bflo(a.y) + bflo(c.y); v[j][3] = ALPHA * bfhi(h.y) + bfhi(a.y) + bfhi(c.y); }
.LBB0_1658:
	s_or_b64 exec, exec, s[10:11]
	s_and_saveexec_b64 s[8:9], s[6:7]
	s_cbranch_execz .LBB0_1636
	s_waitcnt vmcnt(11)
	v_lshlrev_b32_e32 v34, 16, v80
	v_and_b32_e32 v35, 0xffff0000, v80
	s_waitcnt vmcnt(7)
	v_lshlrev_b32_e32 v36, 16, v84
	v_and_b32_e32 v37, 0xffff0000, v84
	v_pk_fma_f32 v[34:35], v[34:35], s[88:89], v[36:37] op_sel_hi:[1,0,1]
	s_waitcnt vmcnt(3)
	v_lshlrev_b32_e32 v36, 16, v82
	v_and_b32_e32 v37, 0xffff0000, v82
	v_pk_add_f32 v[34:35], v[34:35], v[36:37]
	v_lshlrev_b32_e32 v36, 16, v81
	v_and_b32_e32 v37, 0xffff0000, v81
	v_lshlrev_b32_e32 v38, 16, v85
	v_and_b32_e32 v39, 0xffff0000, v85
	v_pk_fma_f32 v[36:37], v[36:37], s[88:89], v[38:39] op_sel_hi:[1,0,1]
	v_lshlrev_b32_e32 v38, 16, v83
	v_and_b32_e32 v39, 0xffff0000, v83
	v_pk_add_f32 v[36:37], v[36:37], v[38:39]
	v_lshlrev_b32_e32 v38, 16, v74
	v_and_b32_e32 v39, 0xffff0000, v74
	v_lshlrev_b32_e32 v40, 16, v78
	v_and_b32_e32 v41, 0xffff0000, v78
	v_pk_fma_f32 v[38:39], v[38:39], s[88:89], v[40:41] op_sel_hi:[1,0,1]
	s_waitcnt vmcnt(2)
	v_lshlrev_b32_e32 v40, 16, v76
	v_and_b32_e32 v41, 0xffff0000, v76
	v_pk_add_f32 v[38:39], v[38:39], v[40:41]
	v_lshlrev_b32_e32 v40, 16, v75
	v_and_b32_e32 v41, 0xffff0000, v75
	v_lshlrev_b32_e32 v42, 16, v79
	v_and_b32_e32 v43, 0xffff0000, v79
	v_pk_fma_f32 v[40:41], v[40:41], s[88:89], v[42:43] op_sel_hi:[1,0,1]
	v_lshlrev_b32_e32 v42, 16, v77
	v_and_b32_e32 v43, 0xffff0000, v77
	v_pk_add_f32 v[40:41], v[40:41], v[42:43]
	v_lshlrev_b32_e32 v42, 16, v66
	v_and_b32_e32 v43, 0xffff0000, v66
	v_lshlrev_b32_e32 v44, 16, v70
	v_and_b32_e32 v45, 0xffff0000, v70
	v_pk_fma_f32 v[42:43], v[42:43], s[88:89], v[44:45] op_sel_hi:[1,0,1]
	s_waitcnt vmcnt(1)
	v_lshlrev_b32_e32 v44, 16, v68
	v_and_b32_e32 v45, 0xffff0000, v68
	v_pk_add_f32 v[72:73], v[42:43], v[44:45]
	v_lshlrev_b32_e32 v42, 16, v67
	v_and_b32_e32 v43, 0xffff0000, v67
	v_lshlrev_b32_e32 v44, 16, v71
	v_and_b32_e32 v45, 0xffff0000, v71
	v_pk_fma_f32 v[42:43], v[42:43], s[88:89], v[44:45] op_sel_hi:[1,0,1]
	v_lshlrev_b32_e32 v44, 16, v69
	v_and_b32_e32 v45, 0xffff0000, v69
	v_pk_add_f32 v[66:67], v[42:43], v[44:45]
	v_lshlrev_b32_e32 v42, 16, v62
	v_and_b32_e32 v43, 0xffff0000, v62
	v_lshlrev_b32_e32 v44, 16, v64
	v_and_b32_e32 v45, 0xffff0000, v64
	v_pk_fma_f32 v[42:43], v[42:43], s[88:89], v[44:45] op_sel_hi:[1,0,1]
	s_waitcnt vmcnt(0)
; __device__ __forceinline__ float bflo(unsigned w) { return __uint_as_float(w << 16); }
; __device__ __forceinline__ float bfhi(unsigned w) { return __uint_as_float(w & 0xFFFF0000u); }
; __device__ __forceinline__ float frsq(float x) { return __builtin_amdgcn_rsqf(x); }
; __device__ __forceinline__ void ln_affine(f32x4 (&v)[4], const LnPar& q) {
;     float s = 0.f;
; #pragma unroll
;     for (int j = 0; j < 4; ++j) s += (v[j][0] + v[j][1]) + (v[j][2] + v[j][3]);
;     const float mean = wave_sum(s) * (1.f / D); float s2 = 0.f;
; #pragma unroll
;     for (int j = 0; j < 4; ++j) { v[j] = v[j] - mean; s2 += (v[j][0] * v[j][0] + v[j][1] * v[j][1]) + (v[j][2] * v[j][2] + v[j][3] * v[j][3]); }
;     const float rstd = frsq(wave_sum(s2) * (1.f / D) + 1e-5f);
; #pragma unroll
;     for (int j = 0; j < 4; ++j) v[j] = v[j] * rstd * q.g[j] + q.b[j];
; }
; __device__ __forceinline__ void ph_ln2(const Params& p, int l, LAS unsigned char* lds, const int wvid) {
;     ...
;                 v[j][0] = ALPHA * bflo(h.x) + bflo(a.x) + bflo(c.x); v[j][1] = ALPHA * bfhi(h.x) + bfhi(a.x) + bfhi(c.x); v[j][2] = ALPHA * bflo(h.y) + bflo(a.y) + bflo(c.y); v[j][3] = ALPHA * bfhi(h.y) + bfhi(a.y) + bfhi(c.y); }
;             ln_affine(v, ln2);
;             if (l == NLAYER - 1) { float* o = p.out + ((size_t)b * SEQ + (t - NMETA)) * D;
; #pragma unroll
;                 for (int j = 0; j < 4; ++j) *(f32x4*)(o + 4 * lane + 256 * j) = v[j]; }
	v_lshlrev_b32_e32 v44, 16, v60
	v_and_b32_e32 v45, 0xffff0000, v60
	v_pk_add_f32 v[68:69], v[42:43], v[44:45]
	v_lshlrev_b32_e32 v42, 16, v63
	v_and_b32_e32 v43, 0xffff0000, v63
	v_lshlrev_b32_e32 v44, 16, v65
	v_and_b32_e32 v45, 0xffff0000, v65
	v_pk_fma_f32 v[42:43], v[42:43], s[88:89], v[44:45] op_sel_hi:[1,0,1]
	v_lshlrev_b32_e32 v44, 16, v61
	v_and_b32_e32 v45, 0xffff0000, v61
	v_pk_add_f32 v[60:61], v[42:43], v[44:45]
	v_mov_b32_e32 v42, v34
	v_mov_b32_e32 v43, v36
	v_mov_b32_e32 v44, v35
	v_mov_b32_e32 v45, v37
	v_pk_add_f32 v[42:43], v[42:43], v[44:45]
	v_mov_b32_e32 v44, v38
	v_mov_b32_e32 v45, v40
	v_mov_b32_e32 v46, v39
	v_mov_b32_e32 v47, v41
	v_pk_add_f32 v[44:45], v[44:45], v[46:47]
	v_add_f32_e32 v0, v42, v43
	v_pk_add_f32 v[44:45], v[44:45], v[44:45] op_sel:[0,1] op_sel_hi:[1,0]
	v_pk_add_f32 v[46:47], v[72:73], v[72:73] op_sel:[0,1] op_sel_hi:[1,0]
	v_pk_add_f32 v[48:49], v[66:67], v[66:67] op_sel:[0,1] op_sel_hi:[1,0]
	v_add_f32_e32 v42, 0, v0
	v_mov_b32_e32 v43, v68
	v_mov_b32_e32 v45, v69
	v_mov_b32_e32 v47, v60
	v_mov_b32_e32 v49, v61
	v_pk_add_f32 v[42:43], v[42:43], v[44:45]
	v_pk_add_f32 v[44:45], v[46:47], v[48:49]
	s_nop 0
	v_pk_add_f32 v[42:43], v[42:43], v[44:45]
	s_nop 0
	v_add_f32_e32 v0, v42, v43
	v_mov_b32_e32 v42, v1
	s_nop 0
	v_add_f32_dpp v0, v0, v0 quad_perm:[1,0,3,2] row_mask:0xf bank_mask:0xf bound_ctrl:1
	s_nop 1
	v_add_f32_dpp v0, v0, v0 quad_perm:[2,3,0,1] row_mask:0xf bank_mask:0xf bound_ctrl:1
	s_nop 1
	v_add_f32_dpp v0, v0, v0 row_half_mirror row_mask:0xf bank_mask:0xf bound_ctrl:1
	s_nop 1
	v_add_f32_dpp v0, v0, v0 row_mirror row_mask:0xf bank_mask:0xf bound_ctrl:1
	s_nop 1
	v_mov_b32_dpp v42, v0 row_bcast:15 row_mask:0xa bank_mask:0xf
	v_add_f32_e32 v0, v0, v42
	v_mov_b32_e32 v42, v1
	s_nop 1
	v_mov_b32_dpp v42, v0 row_bcast:31 row_mask:0xc bank_mask:0xf
	v_add_f32_e32 v0, v0, v42
	s_nop 0
	v_readlane_b32 s6, v0, 63
	s_nop 1
	v_fma_f32 v35, s6, v220, v35
	v_fmac_f32_e32 v34, s6, v220
	v_fma_f32 v37, s6, v220, v37
	v_fmac_f32_e32 v36, s6, v220
	v_pk_mul_f32 v[42:43], v[36:37], v[36:37]
	v_pk_mul_f32 v[44:45], v[34:35], v[34:35]
	v_fma_f32 v39, s6, v220, v39
	v_pk_mov_b32 v[46:47], v[44:45], v[42:43] op_sel:[1,0]
	v_mov_b32_e32 v45, v43
	v_fmac_f32_e32 v38, s6, v220
	v_fma_f32 v41, s6, v220, v41
	v_fmac_f32_e32 v40, s6, v220
	v_pk_add_f32 v[42:43], v[46:47], v[44:45]
	v_pk_mul_f32 v[44:45], v[40:41], v[40:41]
	v_pk_mul_f32 v[46:47], v[38:39], v[38:39]
	v_fmac_f32_e32 v72, s6, v220
	v_pk_mov_b32 v[48:49], v[46:47], v[44:45] op_sel:[1,0]
	v_mov_b32_e32 v47, v45
	v_fma_f32 v73, s6, v220, v73
	v_fmac_f32_e32 v66, s6, v220
	v_mul_f32_e32 v0, v72, v72
	v_pk_add_f32 v[44:45], v[48:49], v[46:47]
	v_fma_f32 v67, s6, v220, v67
	v_pk_fma_f32 v[46:47], v[72:73], v[72:73], v[0:1] op_sel_hi:[1,1,0]
	v_mul_f32_e32 v0, v66, v66
	v_pk_add_f32 v[42:43], v[42:43], v[42:43] op_sel_hi:[0,1]
	v_pk_add_f32 v[44:45], v[44:45], v[44:45] op_sel_hi:[0,1]
	v_pk_fma_f32 v[48:49], v[66:67], v[66:67], v[0:1] op_sel_hi:[1,1,0]
	v_fma_f32 v61, s6, v220, v61
	v_fmac_f32_e32 v60, s6, v220
	v_fma_f32 v69, s6, v220, v69
	v_fmac_f32_e32 v68, s6, v220
	v_mul_f32_e32 v46, v68, v68
	v_mul_f32_e32 v48, v69, v69
	v_mul_f32_e32 v42, v60, v60
	v_mul_f32_e32 v44, v61, v61
	v_pk_add_f32 v[46:47], v[46:47], v[48:49]
	v_pk_add_f32 v[42:43], v[42:43], v[44:45]
	s_nop 0
	v_pk_add_f32 v[42:43], v[46:47], v[42:43]
	s_nop 0
	v_add_f32_e32 v0, v42, v43
	v_mov_b32_e32 v42, v1
	s_nop 0
	v_add_f32_dpp v0, v0, v0 quad_perm:[1,0,3,2] row_mask:0xf bank_mask:0xf bound_ctrl:1
	s_nop 1
	v_add_f32_dpp v0, v0, v0 quad_perm:[2,3,0,1] row_mask:0xf bank_mask:0xf bound_ctrl:1
	s_nop 1
	v_add_f32_dpp v0, v0, v0 row_half_mirror row_mask:0xf bank_mask:0xf bound_ctrl:1
	s_nop 1
	v_add_f32_dpp v0, v0, v0 row_mirror row_mask:0xf bank_mask:0xf bound_ctrl:1
	s_nop 1
	v_mov_b32_dpp v42, v0 row_bcast:15 row_mask:0xa bank_mask:0xf
	v_add_f32_e32 v0, v0, v42
	v_mov_b32_e32 v42, v1
	s_nop 1
	v_mov_b32_dpp v42, v0 row_bcast:31 row_mask:0xc bank_mask:0xf
	v_add_f32_e32 v0, v0, v42
	s_nop 0
	v_readlane_b32 s6, v0, 63
	s_nop 1
	v_fma_f32 v0, s6, v221, v204
	v_rsq_f32_e32 v0, v0
	v_readlane_b32 s6, v255, 10
	v_readlane_b32 s7, v255, 11
	s_andn2_b64 vcc, exec, s[6:7]
	v_pk_mul_f32 v[34:35], v[34:35], v[0:1] op_sel_hi:[1,0]
	v_pk_mul_f32 v[36:37], v[36:37], v[0:1] op_sel_hi:[1,0]
	v_pk_fma_f32 v[46:47], v[2:3], v[34:35], v[6:7]
	v_pk_fma_f32 v[48:49], v[4:5], v[36:37], v[8:9]
	v_pk_mul_f32 v[34:35], v[38:39], v[0:1] op_sel_hi:[1,0]
	v_pk_mul_f32 v[36:37], v[40:41], v[0:1] op_sel_hi:[1,0]
	v_pk_fma_f32 v[42:43], v[10:11], v[34:35], v[14:15]
	v_pk_fma_f32 v[44:45], v[12:13], v[36:37], v[16:17]
	v_pk_mul_f32 v[34:35], v[72:73], v[0:1] op_sel_hi:[1,0]
	v_pk_mul_f32 v[36:37], v[66:67], v[0:1] op_sel_hi:[1,0]
	v_pk_mul_f32 v[38:39], v[68:69], v[0:1] op_sel_hi:[1,0]
	v_pk_mul_f32 v[40:41], v[60:61], v[0:1] op_sel_hi:[1,0]
	v_pk_fma_f32 v[36:37], v[20:21], v[36:37], v[24:25]
	v_pk_fma_f32 v[34:35], v[18:19], v[34:35], v[22:23]
	v_pk_fma_f32 v[40:41], v[28:29], v[40:41], v[32:33]
	v_pk_fma_f32 v[38:39], v[26:27], v[38:39], v[30:31]
	s_mov_b64 s[6:7], -1
	s_cbranch_vccnz .LBB0_1661
	s_mov_b32 s6, 0x7f807f81
	v_mul_hi_i32 v0, v58, s6
	v_lshrrev_b32_e32 v57, 31, v0
	v_ashrrev_i32_e32 v0, 11, v0
	v_add_u32_e32 v60, v0, v57
	v_mul_i32_i24_e32 v0, 0x1010, v60
	v_sub_u32_e32 v62, v58, v0
	v_ashrrev_i32_e32 v61, 31, v60
	v_readlane_b32 s16, v253, 0
	v_ashrrev_i32_e32 v63, 31, v62
	v_lshlrev_b64 v[60:61], 24, v[60:61]
	v_readlane_b32 s18, v253, 2
	v_readlane_b32 s19, v253, 3
	v_lshlrev_b64 v[62:63], 12, v[62:63]
	v_lshlrev_b32_e32 v0, 2, v149
	v_lshl_add_u64 v[60:61], s[18:19], 0, v[60:61]
	v_lshl_add_u64 v[60:61], v[60:61], 0, v[62:63]
	s_mov_b32 s6, 0xffff0000
	v_lshl_add_u64 v[60:61], v[60:61], 0, v[0:1]
	s_mov_b32 s7, -1
	v_lshl_add_u64 v[62:63], v[60:61], 0, s[6:7]
	v_add_co_u32_e32 v60, vcc, 0xffff0000, v60
	s_mov_b64 s[6:7], 0
	s_nop 0
	v_addc_co_u32_e32 v61, vcc, -1, v61, vcc
	v_readlane_b32 s17, v253, 1
	global_store_dwordx4 v[60:61], v[46:49], off nt
	global_store_dwordx4 v[62:63], v[42:45], off offset:1024 nt
	global_store_dwordx4 v[62:63], v[34:37], off offset:2048 nt
	global_store_dwordx4 v[62:63], v[38:41], off offset:3072 nt
